# Fourier stage A/B transposed stores reordered so the two pieces of the same output rows (K then V, p then q) are stored back to back; plus previous changes
# baseline (speedup 1.0000x reference)
;     __device__ __forceinline__ float* tw() const { return (float*)(ws + WS_TW); }
;     __device__ __forceinline__ bf16_t* zm() const { return (bf16_t*)(ws + WS_ZM); }
; __device__ __forceinline__ int v_rd_base(int lane) { return ((lane & 3) << 3) | (((lane >> 2) & 3) << 6) | (((lane >> 4) & 1) << 5) | (((lane >> 5) & 1) << 8); }
; __device__ __forceinline__ void phase_fft_a(const Frame& F) {
;     ...
;         f32x16 zc[2] = {f32x16{}, f32x16{}}, zs[2] = {f32x16{}, f32x16{}};
; #pragma unroll
;         for (int t = 0; t < 2; ++t) {
;             bf16x8 bc[4], bs[4];
; #pragma unroll
;             for (int ks = 0; ks < 4; ++ks) { const int o = k1 * 128 + t * 64 + ks * 16 + hi * 8; bc[ks] = *(const bf16x8*)(dc + o); bs[ks] = *(const bf16x8*)(ds + o); }
;             const int vb = (int)(uintptr_t)img + t * 16384 + ff::v_rd_base(lane) + chh * 1024;
;             ff::xt_two<0>(zc[0], zs[0], vb, bc, bs);
;             ff::xt_two<1>(zc[1], zs[1], vb, bc, bs);
;         }
;         const f32x2 t2 = *(const f32x2*)(F.tw() + (size_t)(k1 * 64 + n2) * 2);
;         bf16_t* zp = F.zm() + (size_t)((b * 128 + k1) * 64 + n2) * DM + cb * 128 + 64 * chh + 4 * hi;
.LBB0_326:
	global_load_dwordx4 v[2:5], v[82:83], off
	global_load_dwordx4 v[18:21], v[84:85], off
	global_load_dwordx4 v[116:119], v[86:87], off
	global_load_dwordx4 v[128:131], v[88:89], off
	global_load_dwordx4 v[132:135], v[90:91], off
	global_load_dwordx4 v[136:139], v[92:93], off
	global_load_dwordx4 v[140:143], v[94:95], off
	global_load_dwordx4 v[148:151], v[96:97], off
	v_add_u32_e32 v115, s30, v123
	ds_read_b64_tr_b16 v[6:7], v115 offset:0
	ds_read_b64_tr_b16 v[8:9], v115 offset:0x800
	ds_read_b64_tr_b16 v[10:11], v115 offset:0x1000
	ds_read_b64_tr_b16 v[12:13], v115 offset:0x1800
	ds_read_b64_tr_b16 v[14:15], v115 offset:0x2000
	ds_read_b64_tr_b16 v[16:17], v115 offset:0x2800
	ds_read_b64_tr_b16 v[22:23], v115 offset:0x3000
	ds_read_b64_tr_b16 v[24:25], v115 offset:0x3800
	s_waitcnt lgkmcnt(0)
	s_bfe_u32 s8, s23, 0x60002
	s_waitcnt vmcnt(7)
	v_mfma_f32_32x32x16_bf16 v[34:49], v[6:9], v[2:5], 0
	s_waitcnt vmcnt(6)
	v_mfma_f32_32x32x16_bf16 v[50:65], v[6:9], v[18:21], 0
	s_waitcnt vmcnt(5)
	v_mfma_f32_32x32x16_bf16 v[34:49], v[10:13], v[116:119], v[34:49]
	s_waitcnt vmcnt(4)
	v_mfma_f32_32x32x16_bf16 v[50:65], v[10:13], v[128:131], v[50:65]
	s_waitcnt vmcnt(3)
	v_mfma_f32_32x32x16_bf16 v[34:49], v[14:17], v[132:135], v[34:49]
	s_waitcnt vmcnt(2)
	v_mfma_f32_32x32x16_bf16 v[50:65], v[14:17], v[136:139], v[50:65]
	s_waitcnt vmcnt(1)
	v_mfma_f32_32x32x16_bf16 v[34:49], v[22:25], v[140:143], v[34:49]
	s_waitcnt vmcnt(0)
	v_mfma_f32_32x32x16_bf16 v[50:65], v[22:25], v[148:151], v[50:65]
	ds_read_b64_tr_b16 v[22:23], v115 offset:0x200
	ds_read_b64_tr_b16 v[24:25], v115 offset:0xa00
	ds_read_b64_tr_b16 v[152:153], v115 offset:0x1200
	ds_read_b64_tr_b16 v[154:155], v115 offset:0x1a00
	ds_read_b64_tr_b16 v[156:157], v115 offset:0x2200
	ds_read_b64_tr_b16 v[158:159], v115 offset:0x2a00
	ds_read_b64_tr_b16 v[160:161], v115 offset:0x3200
	ds_read_b64_tr_b16 v[162:163], v115 offset:0x3a00
	s_waitcnt lgkmcnt(0)
	s_nop 0
	v_mfma_f32_32x32x16_bf16 v[2:17], v[22:25], v[2:5], 0
	v_add_u32_e32 v115, 0x4000, v115
	v_mfma_f32_32x32x16_bf16 v[18:33], v[22:25], v[18:21], 0
	v_mfma_f32_32x32x16_bf16 v[2:17], v[152:155], v[116:119], v[2:17]
	v_mfma_f32_32x32x16_bf16 v[18:33], v[152:155], v[128:131], v[18:33]
	v_mfma_f32_32x32x16_bf16 v[2:17], v[156:159], v[132:135], v[2:17]
	v_mfma_f32_32x32x16_bf16 v[18:33], v[156:159], v[136:139], v[18:33]
	v_mfma_f32_32x32x16_bf16 v[2:17], v[160:163], v[140:143], v[2:17]
	v_mfma_f32_32x32x16_bf16 v[18:33], v[160:163], v[148:151], v[18:33]
	global_load_dwordx4 v[116:119], v[98:99], off
	global_load_dwordx4 v[128:131], v[100:101], off
	global_load_dwordx4 v[132:135], v[102:103], off
	global_load_dwordx4 v[136:139], v[104:105], off
	global_load_dwordx4 v[140:143], v[106:107], off
	global_load_dwordx4 v[148:151], v[108:109], off
	global_load_dwordx4 v[152:155], v[110:111], off
	global_load_dwordx4 v[156:159], v[112:113], off
	ds_read_b64_tr_b16 v[160:161], v115 offset:0
	ds_read_b64_tr_b16 v[162:163], v115 offset:0x800
	ds_read_b64_tr_b16 v[164:165], v115 offset:0x1000
	ds_read_b64_tr_b16 v[166:167], v115 offset:0x1800
	ds_read_b64_tr_b16 v[168:169], v115 offset:0x2000
	ds_read_b64_tr_b16 v[170:171], v115 offset:0x2800
	ds_read_b64_tr_b16 v[172:173], v115 offset:0x3000
	ds_read_b64_tr_b16 v[174:175], v115 offset:0x3800
	s_waitcnt lgkmcnt(0)
	s_waitcnt vmcnt(7)
	v_mfma_f32_32x32x16_bf16 v[34:49], v[160:163], v[116:119], v[34:49]
	s_waitcnt vmcnt(6)
	v_mfma_f32_32x32x16_bf16 v[50:65], v[160:163], v[128:131], v[50:65]
	ds_read_b64_tr_b16 v[160:161], v115 offset:0x200
	ds_read_b64_tr_b16 v[162:163], v115 offset:0xa00
	s_waitcnt vmcnt(5)
	v_mfma_f32_32x32x16_bf16 v[34:49], v[164:167], v[132:135], v[34:49]
	s_waitcnt vmcnt(4)
	v_mfma_f32_32x32x16_bf16 v[50:65], v[164:167], v[136:139], v[50:65]
	ds_read_b64_tr_b16 v[164:165], v115 offset:0x1200
	ds_read_b64_tr_b16 v[166:167], v115 offset:0x1a00
	s_waitcnt vmcnt(3)
	v_mfma_f32_32x32x16_bf16 v[34:49], v[168:171], v[140:143], v[34:49]
	s_waitcnt vmcnt(2)
	v_mfma_f32_32x32x16_bf16 v[50:65], v[168:171], v[148:151], v[50:65]
	ds_read_b64_tr_b16 v[168:169], v115 offset:0x2200
	ds_read_b64_tr_b16 v[170:171], v115 offset:0x2a00
	s_waitcnt vmcnt(1)
	v_mfma_f32_32x32x16_bf16 v[34:49], v[172:175], v[152:155], v[34:49]
	s_waitcnt vmcnt(0)
	v_mfma_f32_32x32x16_bf16 v[50:65], v[172:175], v[156:159], v[50:65]
	ds_read_b64_tr_b16 v[172:173], v115 offset:0x3200
	ds_read_b64_tr_b16 v[174:175], v115 offset:0x3a00
	s_waitcnt lgkmcnt(0)
	v_lshl_or_b32 v115, s8, 3, v126
	v_mfma_f32_32x32x16_bf16 v[2:17], v[160:163], v[116:119], v[2:17]
	global_load_dwordx2 v[116:117], v115, s[40:41]
	s_lshr_b32 s9, s23, 1
	s_and_b32 s9, s9, 0x3ffff80
	v_or_b32_e32 v115, s9, v120
	v_lshl_or_b32 v118, v115, 6, s8
	v_ashrrev_i32_e32 v119, 31, v118
	s_and_b32 s22, s22, 0x180
	v_mfma_f32_32x32x16_bf16 v[18:33], v[160:163], v[128:131], v[18:33]
	v_lshlrev_b64 v[118:119], 11, v[118:119]
	v_mov_b32_e32 v128, v34
	v_mov_b32_e32 v129, v50
	v_mov_b32_e32 v130, v50
	v_mov_b32_e32 v131, v34
	v_mov_b32_e32 v50, v35
	v_mov_b32_e32 v34, v51
	v_mfma_f32_32x32x16_bf16 v[2:17], v[164:167], v[132:135], v[2:17]
	v_mov_b32_e32 v132, v36
	v_mov_b32_e32 v133, v52
	s_lshl_b32 s76, s22, 1
	v_lshl_add_u64 v[118:119], s[24:25], 0, v[118:119]
	v_mov_b32_e32 v134, v52
	v_mov_b32_e32 v135, v36
	v_mov_b32_e32 v52, v37
	v_mov_b32_e32 v36, v53
	v_lshl_add_u64 v[118:119], v[118:119], 0, s[76:77]
	v_mfma_f32_32x32x16_bf16 v[18:33], v[164:167], v[136:139], v[18:33]
	v_mov_b32_e32 v136, v38
	v_mov_b32_e32 v137, v54
	v_mov_b32_e32 v138, v54
	v_mov_b32_e32 v139, v38
	v_mov_b32_e32 v54, v39
	v_mov_b32_e32 v38, v55
	v_lshl_add_u64 v[118:119], s[28:29], 1, v[118:119]
	v_mfma_f32_32x32x16_bf16 v[2:17], v[168:171], v[140:143], v[2:17]
	v_mov_b32_e32 v140, v40
	v_mov_b32_e32 v141, v56
	v_mov_b32_e32 v142, v56
	v_mov_b32_e32 v56, v41
	v_mov_b32_e32 v143, v40
	v_mov_b32_e32 v40, v57
	v_lshl_add_u64 v[118:119], v[118:119], 0, v[146:147]
	v_mfma_f32_32x32x16_bf16 v[18:33], v[168:171], v[148:151], v[18:33]
	s_xor_b32 s0, s0, 1
	s_add_i32 s1, s1, s31
	s_andn2_b64 vcc, exec, s[18:19]
	s_mov_b32 s22, s7
	s_mov_b32 s23, s2
	s_waitcnt vmcnt(0)
; __device__ __forceinline__ unsigned cvt_pk_bf16(float lo, float hi) { unsigned r; asm volatile("v_cvt_pk_bf16_f32 %0, %1, %2" : "=v"(r) : "v"(lo), "v"(hi)); return r; }
; __device__ __forceinline__ void phase_fft_a(const Frame& F) {
;     ...
; #pragma unroll
;         for (int dd = 0; dd < 2; ++dd)
; #pragma unroll
;             for (int g = 0; g < 4; ++g) {
;                 float p[4], q[4];
; #pragma unroll
;                 for (int j = 0; j < 4; ++j) { const float c = zc[dd][4 * g + j], s = zs[dd][4 * g + j]; p[j] = c * t2.x - s * t2.y; q[j] = c * t2.y + s * t2.x; }
;                 u32x2 wp, wq; wp.x = cvt_pk_bf16(p[0], p[1]); wp.y = cvt_pk_bf16(p[2], p[3]); wq.x = cvt_pk_bf16(q[0], q[1]); wq.y = cvt_pk_bf16(q[2], q[3]);
;                 *(u32x2*)(zp + dd * 32 + 8 * g) = wp; *(u32x2*)(zp + 512 + dd * 32 + 8 * g) = wq;
	v_pk_mul_f32 v[50:51], v[50:51], v[116:117]
	v_pk_mul_f32 v[34:35], v[34:35], v[116:117]
	v_pk_mul_f32 v[132:133], v[132:133], v[116:117]
	v_pk_mul_f32 v[128:129], v[128:129], v[116:117]
	v_pk_mul_f32 v[52:53], v[52:53], v[116:117]
	v_pk_mul_f32 v[36:37], v[36:37], v[116:117]
	v_sub_f32_e32 v50, v50, v51
	v_add_f32_e32 v51, v35, v34
	v_sub_f32_e32 v35, v132, v133
	v_pk_mul_f32 v[130:131], v[130:131], v[116:117]
	v_pk_mul_f32 v[134:135], v[134:135], v[116:117]
	v_pk_mul_f32 v[136:137], v[136:137], v[116:117]
	v_pk_mul_f32 v[54:55], v[54:55], v[116:117]
	v_pk_mul_f32 v[38:39], v[38:39], v[116:117]
	v_pk_mul_f32 v[140:141], v[140:141], v[116:117]
	v_pk_mul_f32 v[56:57], v[56:57], v[116:117]
	v_sub_f32_e32 v115, v128, v129
	v_sub_f32_e32 v52, v52, v53
	v_add_f32_e32 v37, v37, v36
	v_cvt_pk_bf16_f32 v34, v115, v50
	v_cvt_pk_bf16_f32 v35, v35, v52
	v_pk_mul_f32 v[138:139], v[138:139], v[116:117]
	v_pk_mul_f32 v[142:143], v[142:143], v[116:117]
	v_pk_mul_f32 v[40:41], v[40:41], v[116:117]
	v_add_f32_e32 v127, v131, v130
	v_add_f32_e32 v128, v135, v134
	v_sub_f32_e32 v53, v136, v137
	v_sub_f32_e32 v54, v54, v55
	v_add_f32_e32 v38, v39, v38
	v_sub_f32_e32 v39, v140, v141
	v_sub_f32_e32 v56, v56, v57
	v_cvt_pk_bf16_f32 v36, v127, v51
	v_cvt_pk_bf16_f32 v37, v128, v37
	ds_write_b64 v176, v[34:35]
	ds_write_b64 v176, v[36:37] offset:128
	v_cvt_pk_bf16_f32 v34, v53, v54
	v_cvt_pk_bf16_f32 v35, v39, v56
	v_add_f32_e32 v129, v139, v138
	v_add_f32_e32 v55, v143, v142
	v_add_f32_e32 v40, v41, v40
	v_cvt_pk_bf16_f32 v36, v129, v38
	v_cvt_pk_bf16_f32 v37, v55, v40
	ds_write_b64 v176, v[34:35] offset:16
	ds_write_b64 v176, v[36:37] offset:144
	v_mov_b32_e32 v34, v42
	v_mov_b32_e32 v35, v58
	v_pk_mul_f32 v[34:35], v[34:35], v[116:117]
	v_mfma_f32_32x32x16_bf16 v[2:17], v[172:175], v[152:155], v[2:17]
	v_sub_f32_e32 v36, v34, v35
	v_mov_b32_e32 v34, v58
	v_mov_b32_e32 v35, v42
	v_mul_f32_e64 v34, v34, v116
	v_mul_f32_e64 v35, v35, v117
	v_mov_b32_e32 v58, v43
	v_add_f32_e32 v37, v35, v34
	v_pk_mul_f32 v[34:35], v[58:59], v[116:117]
	v_mov_b32_e32 v42, v59
	v_sub_f32_e32 v38, v34, v35
	v_pk_mul_f32 v[34:35], v[42:43], v[116:117]
	v_mfma_f32_32x32x16_bf16 v[18:33], v[172:175], v[156:159], v[18:33]
	v_add_f32_e32 v39, v35, v34
	v_mov_b32_e32 v34, v44
	v_mov_b32_e32 v35, v60
	v_mul_f32_e64 v34, v34, v116
	v_mul_f32_e64 v35, v35, v117
	v_sub_f32_e32 v40, v34, v35
	v_mov_b32_e32 v34, v60
	v_mov_b32_e32 v35, v44
	v_pk_mul_f32 v[34:35], v[34:35], v[116:117]
	v_mov_b32_e32 v60, v45
	v_add_f32_e32 v41, v35, v34
	v_pk_mul_f32 v[34:35], v[60:61], v[116:117]
	v_mov_b32_e32 v44, v61
	v_sub_f32_e32 v42, v34, v35
	v_pk_mul_f32 v[34:35], v[44:45], v[116:117]
	s_nop 0
	v_add_f32_e32 v43, v35, v34
	v_cvt_pk_bf16_f32 v34, v36, v38
	v_cvt_pk_bf16_f32 v35, v40, v42
	v_cvt_pk_bf16_f32 v36, v37, v39
	v_cvt_pk_bf16_f32 v37, v41, v43
	ds_write_b64 v176, v[34:35] offset:32
	ds_write_b64 v176, v[36:37] offset:160
	v_mov_b32_e32 v34, v46
	v_mov_b32_e32 v35, v62
	v_pk_mul_f32 v[34:35], v[34:35], v[116:117]
	s_nop 0
	v_sub_f32_e32 v36, v34, v35
	v_mov_b32_e32 v34, v62
	v_mov_b32_e32 v35, v46
	v_pk_mul_f32 v[34:35], v[34:35], v[116:117]
	v_mov_b32_e32 v62, v47
	v_add_f32_e32 v37, v35, v34
	v_pk_mul_f32 v[34:35], v[62:63], v[116:117]
	v_mov_b32_e32 v46, v63
	v_sub_f32_e32 v38, v34, v35
	v_pk_mul_f32 v[34:35], v[46:47], v[116:117]
	s_nop 0
	v_add_f32_e32 v39, v35, v34
	v_mov_b32_e32 v34, v48
	v_mov_b32_e32 v35, v64
	v_pk_mul_f32 v[34:35], v[34:35], v[116:117]
	s_nop 0
	v_sub_f32_e32 v40, v34, v35
	v_mov_b32_e32 v34, v64
	v_mov_b32_e32 v35, v48
	v_pk_mul_f32 v[34:35], v[34:35], v[116:117]
	v_mov_b32_e32 v64, v49
	v_add_f32_e32 v41, v35, v34
	v_pk_mul_f32 v[34:35], v[64:65], v[116:117]
	v_mov_b32_e32 v48, v65
	v_sub_f32_e32 v42, v34, v35
	v_pk_mul_f32 v[34:35], v[48:49], v[116:117]
	s_nop 0
	v_add_f32_e32 v43, v35, v34
	v_cvt_pk_bf16_f32 v34, v36, v38
	v_cvt_pk_bf16_f32 v35, v40, v42
	v_cvt_pk_bf16_f32 v36, v37, v39
	v_cvt_pk_bf16_f32 v37, v41, v43
	ds_write_b64 v176, v[34:35] offset:48
	ds_write_b64 v176, v[36:37] offset:176
	v_mov_b32_e32 v34, v2
	v_mov_b32_e32 v35, v18
	v_pk_mul_f32 v[34:35], v[34:35], v[116:117]
	s_nop 0
	v_sub_f32_e32 v36, v34, v35
	v_mov_b32_e32 v34, v18
	v_mov_b32_e32 v35, v2
	v_mov_b32_e32 v2, v19
	v_pk_mul_f32 v[34:35], v[34:35], v[116:117]
	v_mov_b32_e32 v18, v3
	v_pk_mul_f32 v[2:3], v[2:3], v[116:117]
	v_add_f32_e32 v37, v35, v34
	v_pk_mul_f32 v[34:35], v[18:19], v[116:117]
	v_add_f32_e32 v19, v3, v2
	v_mov_b32_e32 v2, v4
	v_mov_b32_e32 v3, v20
	v_pk_mul_f32 v[2:3], v[2:3], v[116:117]
	v_sub_f32_e32 v18, v34, v35
	v_sub_f32_e32 v34, v2, v3
	v_mov_b32_e32 v2, v20
	v_mov_b32_e32 v3, v4
	v_pk_mul_f32 v[2:3], v[2:3], v[116:117]
	v_mov_b32_e32 v20, v5
	v_add_f32_e32 v35, v3, v2
; __device__ __forceinline__ unsigned cvt_pk_bf16(float lo, float hi) { unsigned r; asm volatile("v_cvt_pk_bf16_f32 %0, %1, %2" : "=v"(r) : "v"(lo), "v"(hi)); return r; }
; __device__ __forceinline__ void phase_fft_a(const Frame& F) {
;     ...
; #pragma unroll
;         for (int dd = 0; dd < 2; ++dd)
; #pragma unroll
;             for (int g = 0; g < 4; ++g) {
;                 float p[4], q[4];
; #pragma unroll
;                 for (int j = 0; j < 4; ++j) { const float c = zc[dd][4 * g + j], s = zs[dd][4 * g + j]; p[j] = c * t2.x - s * t2.y; q[j] = c * t2.y + s * t2.x; }
;                 u32x2 wp, wq; wp.x = cvt_pk_bf16(p[0], p[1]); wp.y = cvt_pk_bf16(p[2], p[3]); wq.x = cvt_pk_bf16(q[0], q[1]); wq.y = cvt_pk_bf16(q[2], q[3]);
;                 *(u32x2*)(zp + dd * 32 + 8 * g) = wp; *(u32x2*)(zp + 512 + dd * 32 + 8 * g) = wq;
	v_pk_mul_f32 v[2:3], v[20:21], v[116:117]
	v_mov_b32_e32 v4, v21
	v_sub_f32_e32 v20, v2, v3
	v_pk_mul_f32 v[2:3], v[4:5], v[116:117]
	s_nop 0
	v_add_f32_e32 v5, v3, v2
	v_cvt_pk_bf16_f32 v2, v36, v18
	v_cvt_pk_bf16_f32 v3, v34, v20
	v_cvt_pk_bf16_f32 v4, v37, v19
	v_cvt_pk_bf16_f32 v5, v35, v5
	ds_write_b64 v176, v[2:3] offset:64
	ds_write_b64 v176, v[4:5] offset:192
	v_mov_b32_e32 v2, v6
	v_mov_b32_e32 v3, v22
	v_pk_mul_f32 v[2:3], v[2:3], v[116:117]
	s_nop 0
	v_sub_f32_e32 v4, v2, v3
	v_mov_b32_e32 v2, v22
	v_mov_b32_e32 v3, v6
	v_pk_mul_f32 v[2:3], v[2:3], v[116:117]
	v_mov_b32_e32 v22, v7
	v_add_f32_e32 v5, v3, v2
	v_pk_mul_f32 v[2:3], v[22:23], v[116:117]
	v_mov_b32_e32 v6, v23
	v_sub_f32_e32 v18, v2, v3
	v_pk_mul_f32 v[2:3], v[6:7], v[116:117]
	s_nop 0
	v_add_f32_e32 v6, v3, v2
	v_mov_b32_e32 v2, v8
	v_mov_b32_e32 v3, v24
	v_pk_mul_f32 v[2:3], v[2:3], v[116:117]
	s_nop 0
	v_sub_f32_e32 v7, v2, v3
	v_mov_b32_e32 v2, v24
	v_mov_b32_e32 v3, v8
	v_pk_mul_f32 v[2:3], v[2:3], v[116:117]
	v_mov_b32_e32 v24, v9
	v_add_f32_e32 v19, v3, v2
	v_pk_mul_f32 v[2:3], v[24:25], v[116:117]
	v_mov_b32_e32 v8, v25
	v_sub_f32_e32 v20, v2, v3
	v_pk_mul_f32 v[2:3], v[8:9], v[116:117]
	s_nop 0
	v_add_f32_e32 v8, v3, v2
	v_cvt_pk_bf16_f32 v2, v4, v18
	v_cvt_pk_bf16_f32 v3, v7, v20
	v_cvt_pk_bf16_f32 v4, v5, v6
	v_cvt_pk_bf16_f32 v5, v19, v8
	ds_write_b64 v176, v[2:3] offset:80
	ds_write_b64 v176, v[4:5] offset:208
	v_mov_b32_e32 v2, v10
	v_mov_b32_e32 v3, v26
	v_pk_mul_f32 v[2:3], v[2:3], v[116:117]
	s_nop 0
	v_sub_f32_e32 v4, v2, v3
	v_mov_b32_e32 v2, v26
	v_mov_b32_e32 v3, v10
	v_pk_mul_f32 v[2:3], v[2:3], v[116:117]
	v_mov_b32_e32 v26, v11
	v_add_f32_e32 v5, v3, v2
	v_pk_mul_f32 v[2:3], v[26:27], v[116:117]
	v_mov_b32_e32 v10, v27
	v_sub_f32_e32 v6, v2, v3
	v_pk_mul_f32 v[2:3], v[10:11], v[116:117]
	s_nop 0
	v_add_f32_e32 v7, v3, v2
	v_mov_b32_e32 v2, v12
	v_mov_b32_e32 v3, v28
	v_pk_mul_f32 v[2:3], v[2:3], v[116:117]
	s_nop 0
	v_sub_f32_e32 v8, v2, v3
	v_mov_b32_e32 v2, v28
	v_mov_b32_e32 v3, v12
	v_pk_mul_f32 v[2:3], v[2:3], v[116:117]
	v_mov_b32_e32 v28, v13
	v_add_f32_e32 v9, v3, v2
	v_pk_mul_f32 v[2:3], v[28:29], v[116:117]
	v_mov_b32_e32 v12, v29
	v_sub_f32_e32 v10, v2, v3
	v_pk_mul_f32 v[2:3], v[12:13], v[116:117]
	s_nop 0
	v_add_f32_e32 v11, v3, v2
	v_cvt_pk_bf16_f32 v2, v4, v6
	v_cvt_pk_bf16_f32 v3, v8, v10
	v_cvt_pk_bf16_f32 v4, v5, v7
	v_cvt_pk_bf16_f32 v5, v9, v11
	ds_write_b64 v176, v[2:3] offset:96
	ds_write_b64 v176, v[4:5] offset:224
	v_mov_b32_e32 v2, v14
	v_mov_b32_e32 v3, v30
	v_pk_mul_f32 v[2:3], v[2:3], v[116:117]
	s_nop 0
	v_sub_f32_e32 v4, v2, v3
	v_mov_b32_e32 v2, v30
	v_mov_b32_e32 v3, v14
	v_pk_mul_f32 v[2:3], v[2:3], v[116:117]
	v_mov_b32_e32 v30, v15
	v_add_f32_e32 v5, v3, v2
	v_pk_mul_f32 v[2:3], v[30:31], v[116:117]
	v_mov_b32_e32 v14, v31
	v_sub_f32_e32 v6, v2, v3
	v_pk_mul_f32 v[2:3], v[14:15], v[116:117]
	s_nop 0
	v_add_f32_e32 v7, v3, v2
	v_mov_b32_e32 v2, v16
	v_mov_b32_e32 v3, v32
	v_pk_mul_f32 v[2:3], v[2:3], v[116:117]
	s_nop 0
	v_sub_f32_e32 v8, v2, v3
	v_mov_b32_e32 v2, v32
	v_mov_b32_e32 v3, v16
	v_pk_mul_f32 v[2:3], v[2:3], v[116:117]
	v_mov_b32_e32 v32, v17
	v_add_f32_e32 v9, v3, v2
	v_pk_mul_f32 v[2:3], v[32:33], v[116:117]
	v_mov_b32_e32 v16, v33
	v_sub_f32_e32 v10, v2, v3
	v_pk_mul_f32 v[2:3], v[16:17], v[116:117]
	s_nop 0
	v_add_f32_e32 v11, v3, v2
	v_cvt_pk_bf16_f32 v2, v4, v6
	v_cvt_pk_bf16_f32 v3, v8, v10
	v_cvt_pk_bf16_f32 v4, v5, v7
	v_cvt_pk_bf16_f32 v5, v9, v11
	ds_write_b64 v176, v[2:3] offset:112
	ds_write_b64 v176, v[4:5] offset:240
	s_waitcnt lgkmcnt(0)
	ds_read_b128 v[184:187], v177
	ds_read_b128 v[202:205], v177 offset:128
	ds_read_b128 v[188:191], v177 offset:2176
	ds_read_b128 v[206:209], v177 offset:2304
	ds_read_b128 v[192:195], v177 offset:4352
	ds_read_b128 v[210:213], v177 offset:4480
	ds_read_b128 v[198:201], v177 offset:6528
	ds_read_b128 v[214:217], v177 offset:6656
	s_mov_b64 s[100:101], 0x100000
	v_lshl_add_u64 v[178:179], v[118:119], 0, s[100:101]
	v_lshl_add_u64 v[180:181], v[178:179], 0, s[100:101]
	v_lshl_add_u64 v[182:183], v[180:181], 0, s[100:101]
	s_waitcnt lgkmcnt(7)
	global_store_dwordx4 v[118:119], v[184:187], off
	s_waitcnt lgkmcnt(6)
	global_store_dwordx4 v[118:119], v[202:205], off offset:1024
	s_waitcnt lgkmcnt(5)
	global_store_dwordx4 v[178:179], v[188:191], off
	s_waitcnt lgkmcnt(4)
	global_store_dwordx4 v[178:179], v[206:209], off offset:1024
	s_waitcnt lgkmcnt(3)
	global_store_dwordx4 v[180:181], v[192:195], off
	s_waitcnt lgkmcnt(2)
	global_store_dwordx4 v[180:181], v[210:213], off offset:1024
	s_waitcnt lgkmcnt(1)
	global_store_dwordx4 v[182:183], v[198:201], off
	s_waitcnt lgkmcnt(0)
	global_store_dwordx4 v[182:183], v[214:217], off offset:1024
	s_cbranch_vccz .LBB0_331

; __device__ __forceinline__ unsigned cvt_pk_bf16(float lo, float hi) { unsigned r; asm volatile("v_cvt_pk_bf16_f32 %0, %1, %2" : "=v"(r) : "v"(lo), "v"(hi)); return r; }
;     __device__ __forceinline__ bf16_t* proj() const { return (bf16_t*)(ws + WS_PROJ); }
; __device__ __forceinline__ int v_rd_base(int lane) { return ((lane & 3) << 3) | (((lane >> 2) & 3) << 6) | (((lane >> 4) & 1) << 5) | (((lane >> 5) & 1) << 8); }
; __device__ __forceinline__ void phase_fft_b(const Frame& F) {
;     ...
;         f32x16 ar = f32x16{}, bi = f32x16{};
;         const int vbP = (int)(uintptr_t)img + ff::v_rd_base(lane) + cq * 512;
;         ff::xt_two<0>(ar, bi, vbP, bc, bs);
;         ff::xt_two<0>(ar, bi, vbP + 16384, bn, bc);
;         bf16_t* op = F.proj() + (size_t)(b * SEQ + k1 + 128 * k2) * INW + cb * 128 + 32 * cq + 4 * hi;
; #pragma unroll
;         for (int g = 0; g < 4; ++g) {
;             u32x2 wa, wb;
;             wa.x = cvt_pk_bf16(ar[4 * g] * 0.011048543456039806f, ar[4 * g + 1] * 0.011048543456039806f); wa.y = cvt_pk_bf16(ar[4 * g + 2] * 0.011048543456039806f, ar[4 * g + 3] * 0.011048543456039806f);
;             wb.x = cvt_pk_bf16(bi[4 * g] * 0.011048543456039806f, bi[4 * g + 1] * 0.011048543456039806f); wb.y = cvt_pk_bf16(bi[4 * g + 2] * 0.011048543456039806f, bi[4 * g + 3] * 0.011048543456039806f);
;             *(u32x2*)(op + C_K + 8 * g) = wa; *(u32x2*)(op + C_V + 8 * g) = wb;
;         }
.LBB0_511:
	v_add_u32_e32 v99, s40, v103
	ds_read_b64_tr_b16 v[2:3], v99 offset:0
	ds_read_b64_tr_b16 v[4:5], v99 offset:0x800
	ds_read_b64_tr_b16 v[106:107], v99 offset:0x1000
	ds_read_b64_tr_b16 v[108:109], v99 offset:0x1800
	ds_read_b64_tr_b16 v[110:111], v99 offset:0x2000
	ds_read_b64_tr_b16 v[112:113], v99 offset:0x2800
	ds_read_b64_tr_b16 v[114:115], v99 offset:0x3000
	ds_read_b64_tr_b16 v[116:117], v99 offset:0x3800
	s_waitcnt lgkmcnt(0)
	s_bfe_u32 s28, s31, 0x70002
	v_mfma_f32_32x32x16_bf16 v[18:33], v[2:5], v[34:37], 0
	v_add_u32_e32 v99, 0x4000, v99
	v_mfma_f32_32x32x16_bf16 v[2:17], v[2:5], v[38:41], 0
	v_mfma_f32_32x32x16_bf16 v[18:33], v[106:109], v[46:49], v[18:33]
	v_mfma_f32_32x32x16_bf16 v[2:17], v[106:109], v[50:53], v[2:17]
	ds_read_b64_tr_b16 v[106:107], v99 offset:0
	ds_read_b64_tr_b16 v[108:109], v99 offset:0x800
	v_mfma_f32_32x32x16_bf16 v[18:33], v[110:113], v[58:61], v[18:33]
	v_mfma_f32_32x32x16_bf16 v[2:17], v[110:113], v[62:65], v[2:17]
	ds_read_b64_tr_b16 v[110:111], v99 offset:0x1000
	ds_read_b64_tr_b16 v[112:113], v99 offset:0x1800
	v_mfma_f32_32x32x16_bf16 v[18:33], v[114:117], v[70:73], v[18:33]
	v_mfma_f32_32x32x16_bf16 v[2:17], v[114:117], v[74:77], v[2:17]
	ds_read_b64_tr_b16 v[114:115], v99 offset:0x2000
	ds_read_b64_tr_b16 v[116:117], v99 offset:0x2800
	ds_read_b64_tr_b16 v[118:119], v99 offset:0x3000
	ds_read_b64_tr_b16 v[120:121], v99 offset:0x3800
	s_waitcnt lgkmcnt(0)
	v_mfma_f32_32x32x16_bf16 v[18:33], v[106:109], v[42:45], v[18:33]
	s_and_b32 s29, s1, 0xffffe000
	s_or_b32 s28, s29, s28
	s_xor_b32 s0, s0, 1
	s_andn2_b64 vcc, exec, s[24:25]
	s_mov_b32 s31, s2
	v_mfma_f32_32x32x16_bf16 v[2:17], v[106:109], v[34:37], v[2:17]
	v_or_b32_e32 v106, s28, v1
	v_ashrrev_i32_e32 v107, 31, v106
	v_lshlrev_b64 v[106:107], 13, v[106:107]
	s_and_b32 s28, s30, 0x180
	v_lshl_add_u64 v[106:107], s[22:23], 0, v[106:107]
	s_lshl_b32 s76, s28, 1
	v_lshl_add_u64 v[106:107], v[106:107], 0, s[76:77]
	v_mfma_f32_32x32x16_bf16 v[18:33], v[110:113], v[54:57], v[18:33]
	v_lshl_add_u64 v[106:107], s[18:19], 1, v[106:107]
	v_lshl_add_u64 v[106:107], v[106:107], 0, v[146:147]
	v_readlane_b32 s28, v254, 7
	s_add_i32 s1, s1, s28
	s_mov_b32 s30, s7
	v_mfma_f32_32x32x16_bf16 v[2:17], v[110:113], v[46:49], v[2:17]
	v_mfma_f32_32x32x16_bf16 v[18:33], v[114:117], v[66:69], v[18:33]
	v_mfma_f32_32x32x16_bf16 v[2:17], v[114:117], v[58:61], v[2:17]
	v_mfma_f32_32x32x16_bf16 v[18:33], v[118:121], v[78:81], v[18:33]
	v_mfma_f32_32x32x16_bf16 v[2:17], v[118:121], v[70:73], v[2:17]
	s_nop 10
	v_mul_f32_e32 v18, 0x3c3504f3, v18
	v_mul_f32_e32 v19, 0x3c3504f3, v19
	v_mul_f32_e32 v20, 0x3c3504f3, v20
	v_mul_f32_e32 v21, 0x3c3504f3, v21
	v_cvt_pk_bf16_f32 v166, v18, v19
	v_cvt_pk_bf16_f32 v167, v20, v21
	ds_write_b64 v122, v[166:167]
	v_mul_f32_e32 v2, 0x3c3504f3, v2
	v_mul_f32_e32 v3, 0x3c3504f3, v3
	v_mul_f32_e32 v4, 0x3c3504f3, v4
	v_mul_f32_e32 v5, 0x3c3504f3, v5
	v_cvt_pk_bf16_f32 v168, v2, v3
	v_cvt_pk_bf16_f32 v169, v4, v5
	ds_write_b64 v122, v[168:169] offset:64
	v_mul_f32_e32 v22, 0x3c3504f3, v22
	v_mul_f32_e32 v23, 0x3c3504f3, v23
	v_mul_f32_e32 v24, 0x3c3504f3, v24
	v_mul_f32_e32 v25, 0x3c3504f3, v25
	v_cvt_pk_bf16_f32 v170, v22, v23
	v_cvt_pk_bf16_f32 v171, v24, v25
	ds_write_b64 v122, v[170:171] offset:16
	v_mul_f32_e32 v6, 0x3c3504f3, v6
	v_mul_f32_e32 v7, 0x3c3504f3, v7
	v_mul_f32_e32 v8, 0x3c3504f3, v8
	v_mul_f32_e32 v9, 0x3c3504f3, v9
	v_cvt_pk_bf16_f32 v172, v6, v7
	v_cvt_pk_bf16_f32 v173, v8, v9
	ds_write_b64 v122, v[172:173] offset:80
	v_mul_f32_e32 v26, 0x3c3504f3, v26
	v_mul_f32_e32 v27, 0x3c3504f3, v27
	v_mul_f32_e32 v28, 0x3c3504f3, v28
	v_mul_f32_e32 v29, 0x3c3504f3, v29
	v_cvt_pk_bf16_f32 v174, v26, v27
	v_cvt_pk_bf16_f32 v175, v28, v29
	ds_write_b64 v122, v[174:175] offset:32
	v_mul_f32_e32 v10, 0x3c3504f3, v10
	v_mul_f32_e32 v11, 0x3c3504f3, v11
	v_mul_f32_e32 v12, 0x3c3504f3, v12
	v_mul_f32_e32 v13, 0x3c3504f3, v13
	v_cvt_pk_bf16_f32 v176, v10, v11
	v_cvt_pk_bf16_f32 v177, v12, v13
	ds_write_b64 v122, v[176:177] offset:96
	v_mul_f32_e32 v30, 0x3c3504f3, v30
	v_mul_f32_e32 v31, 0x3c3504f3, v31
	v_mul_f32_e32 v32, 0x3c3504f3, v32
	v_mul_f32_e32 v33, 0x3c3504f3, v33
	v_cvt_pk_bf16_f32 v178, v30, v31
	v_cvt_pk_bf16_f32 v179, v32, v33
	ds_write_b64 v122, v[178:179] offset:48
	v_mul_f32_e32 v14, 0x3c3504f3, v14
	v_mul_f32_e32 v15, 0x3c3504f3, v15
	v_mul_f32_e32 v16, 0x3c3504f3, v16
	v_mul_f32_e32 v17, 0x3c3504f3, v17
	v_cvt_pk_bf16_f32 v180, v14, v15
	v_cvt_pk_bf16_f32 v181, v16, v17
	ds_write_b64 v122, v[180:181] offset:112
	s_waitcnt lgkmcnt(0)
	ds_read_b128 v[150:153], v123
	ds_read_b128 v[158:161], v123 offset:64
	ds_read_b128 v[154:157], v123 offset:2304
	ds_read_b128 v[162:165], v123 offset:2368
	s_mov_b64 s[28:29], 0x1000000
	v_lshl_add_u64 v[124:125], v[106:107], 0, s[28:29]
	s_waitcnt lgkmcnt(2)
	global_store_dwordx4 v[106:107], v[150:153], off offset:1024
	global_store_dwordx4 v[106:107], v[158:161], off offset:2048
	s_waitcnt lgkmcnt(0)
	global_store_dwordx4 v[124:125], v[154:157], off offset:1024
	global_store_dwordx4 v[124:125], v[162:165], off offset:2048
	s_cbranch_vccz .LBB0_516
